# grid barrier: non-leader acquire (buffer_inv) issued before the generation spin instead of after
# speedup vs baseline: 1.0118x; 1.0118x over previous
.LBB0_88:
	s_or_b64 exec, exec, s[8:9]
	v_cvt_f32_u32_e32 v4, v2
	s_waitcnt vmcnt(0)
	v_readfirstlane_b32 s3, v3
	v_sub_u32_e32 v3, 0, v2
	v_rcp_iflag_f32_e32 v4, v4
	v_add_u32_e32 v5, s3, v1
	v_mul_f32_e32 v4, 0x4f7ffffe, v4
	v_cvt_u32_f32_e32 v4, v4
	v_mul_lo_u32 v1, v3, v4
	v_mul_hi_u32 v1, v4, v1
	v_add_u32_e32 v1, v4, v1
	v_mul_hi_u32 v1, v5, v1
	v_mul_lo_u32 v3, v1, v2
	v_sub_u32_e32 v3, v5, v3
	v_add_u32_e32 v4, 1, v1
	v_cmp_ge_u32_e32 vcc, v3, v2
	s_nop 1
	v_cndmask_b32_e32 v1, v1, v4, vcc
	v_sub_u32_e32 v4, v3, v2
	v_cndmask_b32_e32 v3, v3, v4, vcc
	v_add_u32_e32 v4, 1, v1
	v_cmp_ge_u32_e32 vcc, v3, v2
	v_add_u32_e32 v3, 1, v5
	s_nop 0
	v_cndmask_b32_e32 v1, v1, v4, vcc
	v_mul_lo_u32 v4, v2, v1
	v_add_u32_e32 v2, v4, v2
	v_cmp_ne_u32_e32 vcc, v3, v2
	s_and_saveexec_b64 s[6:7], vcc
	s_xor_b64 s[6:7], exec, s[6:7]
	s_cbranch_execz .LBB0_102
	s_add_i32 s8, s2, 0x900
	s_mov_b32 s9, 0
	s_lshl_b64 s[8:9], s[8:9], 2
	s_add_u32 s10, s4, s8
	s_addc_u32 s11, s5, s9
	s_waitcnt lgkmcnt(0)
	v_mov_b32_e32 v0, 0
	buffer_inv sc1
	global_load_dword v2, v0, s[10:11] sc1
	s_waitcnt vmcnt(0)
	v_cmp_eq_u32_e32 vcc, v2, v1
	s_and_saveexec_b64 s[8:9], vcc
	s_cbranch_execz .LBB0_101
	s_mov_b32 s3, 1
	s_mov_b64 s[12:13], 0
	s_branch .LBB0_92

.LBB0_101:
	s_or_b64 exec, exec, s[8:9]
	s_waitcnt vmcnt(0)
	s_waitcnt vmcnt(0)

.LBB0_192:
	s_or_b64 exec, exec, s[8:9]
	v_cvt_f32_u32_e32 v5, v3
	s_waitcnt vmcnt(0)
	v_readfirstlane_b32 s3, v4
	v_sub_u32_e32 v4, 0, v3
	v_rcp_iflag_f32_e32 v5, v5
	v_add_u32_e32 v6, s3, v1
	v_mul_f32_e32 v5, 0x4f7ffffe, v5
	v_cvt_u32_f32_e32 v5, v5
	v_mul_lo_u32 v1, v4, v5
	v_mul_hi_u32 v1, v5, v1
	v_add_u32_e32 v1, v5, v1
	v_mul_hi_u32 v1, v6, v1
	v_mul_lo_u32 v4, v1, v3
	v_sub_u32_e32 v4, v6, v4
	v_add_u32_e32 v5, 1, v1
	v_cmp_ge_u32_e32 vcc, v4, v3
	s_nop 1
	v_cndmask_b32_e32 v1, v1, v5, vcc
	v_sub_u32_e32 v5, v4, v3
	v_cndmask_b32_e32 v4, v4, v5, vcc
	v_add_u32_e32 v5, 1, v1
	v_cmp_ge_u32_e32 vcc, v4, v3
	v_add_u32_e32 v4, 1, v6
	s_nop 0
	v_cndmask_b32_e32 v1, v1, v5, vcc
	v_mul_lo_u32 v5, v3, v1
	v_add_u32_e32 v3, v5, v3
	v_cmp_ne_u32_e32 vcc, v4, v3
	s_and_saveexec_b64 s[6:7], vcc
	s_xor_b64 s[6:7], exec, s[6:7]
	s_cbranch_execz .LBB0_206
	s_add_i32 s24, s2, 0x900
	s_lshl_b64 s[8:9], s[24:25], 2
	s_add_u32 s12, s4, s8
	s_addc_u32 s13, s5, s9
	s_waitcnt lgkmcnt(0)
	buffer_inv sc1
	global_load_dword v2, v0, s[12:13] sc1
	s_waitcnt vmcnt(0)
	v_cmp_eq_u32_e32 vcc, v2, v1
	s_and_saveexec_b64 s[8:9], vcc
	s_cbranch_execz .LBB0_205
	s_mov_b32 s3, 1
	s_mov_b64 s[14:15], 0
	s_branch .LBB0_196

.LBB0_504:
	s_or_b64 exec, exec, s[12:13]
	v_cvt_f32_u32_e32 v5, v3
	s_waitcnt vmcnt(0)
	v_readfirstlane_b32 s3, v4
	v_sub_u32_e32 v4, 0, v3
	v_rcp_iflag_f32_e32 v5, v5
	v_add_u32_e32 v6, s3, v1
	v_mul_f32_e32 v5, 0x4f7ffffe, v5
	v_cvt_u32_f32_e32 v5, v5
	v_mul_lo_u32 v1, v4, v5
	v_mul_hi_u32 v1, v5, v1
	v_add_u32_e32 v1, v5, v1
	v_mul_hi_u32 v1, v6, v1
	v_mul_lo_u32 v4, v1, v3
	v_sub_u32_e32 v4, v6, v4
	v_add_u32_e32 v5, 1, v1
	v_cmp_ge_u32_e32 vcc, v4, v3
	s_nop 1
	v_cndmask_b32_e32 v1, v1, v5, vcc
	v_sub_u32_e32 v5, v4, v3
	v_cndmask_b32_e32 v4, v4, v5, vcc
	v_add_u32_e32 v5, 1, v1
	v_cmp_ge_u32_e32 vcc, v4, v3
	v_add_u32_e32 v4, 1, v6
	s_nop 0
	v_cndmask_b32_e32 v1, v1, v5, vcc
	v_mul_lo_u32 v5, v3, v1
	v_add_u32_e32 v3, v5, v3
	v_cmp_ne_u32_e32 vcc, v4, v3
	s_and_saveexec_b64 s[6:7], vcc
	s_xor_b64 s[6:7], exec, s[6:7]
	s_cbranch_execz .LBB0_518
	s_add_i32 s24, s2, 0x900
	s_lshl_b64 s[8:9], s[24:25], 2
	s_add_u32 s16, s4, s8
	s_addc_u32 s17, s5, s9
	s_waitcnt lgkmcnt(0)
	buffer_inv sc1
	global_load_dword v2, v0, s[16:17] sc1
	s_waitcnt vmcnt(0)
	v_cmp_eq_u32_e32 vcc, v2, v1
	s_and_saveexec_b64 s[12:13], vcc
	s_cbranch_execz .LBB0_517
	s_mov_b32 s3, 1
	s_mov_b64 s[20:21], 0
	s_branch .LBB0_508

.LBB0_517:
	s_or_b64 exec, exec, s[12:13]
	s_waitcnt vmcnt(0)
	s_waitcnt vmcnt(0)

.LBB0_728:
	s_or_b64 exec, exec, s[8:9]
	v_cvt_f32_u32_e32 v5, v3
	s_waitcnt vmcnt(0)
	v_readfirstlane_b32 s3, v4
	v_sub_u32_e32 v4, 0, v3
	v_rcp_iflag_f32_e32 v5, v5
	v_add_u32_e32 v6, s3, v1
	v_mul_f32_e32 v5, 0x4f7ffffe, v5
	v_cvt_u32_f32_e32 v5, v5
	v_mul_lo_u32 v1, v4, v5
	v_mul_hi_u32 v1, v5, v1
	v_add_u32_e32 v1, v5, v1
	v_mul_hi_u32 v1, v6, v1
	v_mul_lo_u32 v4, v1, v3
	v_sub_u32_e32 v4, v6, v4
	v_add_u32_e32 v5, 1, v1
	v_cmp_ge_u32_e32 vcc, v4, v3
	s_nop 1
	v_cndmask_b32_e32 v1, v1, v5, vcc
	v_sub_u32_e32 v5, v4, v3
	v_cndmask_b32_e32 v4, v4, v5, vcc
	v_add_u32_e32 v5, 1, v1
	v_cmp_ge_u32_e32 vcc, v4, v3
	v_add_u32_e32 v4, 1, v6
	s_nop 0
	v_cndmask_b32_e32 v1, v1, v5, vcc
	v_mul_lo_u32 v5, v3, v1
	v_add_u32_e32 v3, v5, v3
	v_cmp_ne_u32_e32 vcc, v4, v3
	s_and_saveexec_b64 s[6:7], vcc
	s_xor_b64 s[6:7], exec, s[6:7]
	s_cbranch_execz .LBB0_742
	s_add_i32 s24, s2, 0x900
	s_lshl_b64 s[8:9], s[24:25], 2
	s_add_u32 s12, s4, s8
	s_addc_u32 s13, s5, s9
	s_waitcnt lgkmcnt(0)
	buffer_inv sc1
	global_load_dword v2, v0, s[12:13] sc1
	s_waitcnt vmcnt(0)
	v_cmp_eq_u32_e32 vcc, v2, v1
	s_and_saveexec_b64 s[8:9], vcc
	s_cbranch_execz .LBB0_741
	s_mov_b32 s3, 1
	s_mov_b64 s[16:17], 0
	s_branch .LBB0_732

.LBB0_994:
	s_or_b64 exec, exec, s[8:9]
	v_cvt_f32_u32_e32 v5, v3
	s_waitcnt vmcnt(0)
	v_readfirstlane_b32 s3, v4
	v_sub_u32_e32 v4, 0, v3
	v_rcp_iflag_f32_e32 v5, v5
	v_add_u32_e32 v6, s3, v1
	v_mul_f32_e32 v5, 0x4f7ffffe, v5
	v_cvt_u32_f32_e32 v5, v5
	v_mul_lo_u32 v1, v4, v5
	v_mul_hi_u32 v1, v5, v1
	v_add_u32_e32 v1, v5, v1
	v_mul_hi_u32 v1, v6, v1
	v_mul_lo_u32 v4, v1, v3
	v_sub_u32_e32 v4, v6, v4
	v_add_u32_e32 v5, 1, v1
	v_cmp_ge_u32_e32 vcc, v4, v3
	s_nop 1
	v_cndmask_b32_e32 v1, v1, v5, vcc
	v_sub_u32_e32 v5, v4, v3
	v_cndmask_b32_e32 v4, v4, v5, vcc
	v_add_u32_e32 v5, 1, v1
	v_cmp_ge_u32_e32 vcc, v4, v3
	v_add_u32_e32 v4, 1, v6
	s_nop 0
	v_cndmask_b32_e32 v1, v1, v5, vcc
	v_mul_lo_u32 v5, v3, v1
	v_add_u32_e32 v3, v5, v3
	v_cmp_ne_u32_e32 vcc, v4, v3
	s_and_saveexec_b64 s[6:7], vcc
	s_xor_b64 s[6:7], exec, s[6:7]
	s_cbranch_execz .LBB0_1008
	s_add_i32 s24, s2, 0x900
	s_lshl_b64 s[8:9], s[24:25], 2
	s_add_u32 s10, s4, s8
	s_addc_u32 s11, s5, s9
	s_waitcnt lgkmcnt(0)
	buffer_inv sc1
	global_load_dword v2, v0, s[10:11] sc1
	s_waitcnt vmcnt(0)
	v_cmp_eq_u32_e32 vcc, v2, v1
	s_and_saveexec_b64 s[8:9], vcc
	s_cbranch_execz .LBB0_1007
	s_mov_b32 s3, 1
	s_mov_b64 s[12:13], 0
	s_branch .LBB0_998
